# baseline (speedup 1.0000x reference)
_Z13qkv256_kernelPcPKfS1_:
	s_load_dwordx2 s[8:9], s[0:1], 0x0
	s_and_b32 s6, s2, 7
	s_ashr_i32 s16, s2, 3
	s_cmp_lt_i32 s16, 20
	s_cbranch_scc0 .LBB1_2
	s_cmp_lt_u32 s16, 16
	s_cbranch_scc0 .Lq_enc
	s_lshl_b32 s3, s6, 4
	s_movk_i32 s7, 0x100
	s_branch .LBB1_4
.Lq_enc:
	s_cmp_lt_u32 s16, 18
	s_cbranch_scc0 .Lq_ev
	s_mul_i32 s3, s16, 7
	s_add_u32 s3, s3, s6
	s_movk_i32 s7, 0x100
	s_branch .LBB1_4
.Lq_ev:
	s_lshl_b32 s3, s6, 1
	s_movk_i32 s7, 0x17e
	s_branch .LBB1_4
